# attention block selection: 16-round wave-max top-k replaced by a radix select on the same packed keys (same selected set)
# speedup vs baseline: 1.0215x; 1.0090x over previous
; #define LAS __attribute__((address_space(3)))
; __device__ __forceinline__ void attn_unit(const Frame& F, unsigned char* ws, int g, int qt) {
;     ...
;         unsigned key0[8], key1[8], w0[8], w1[8], w2[8], w3[8];
; #pragma unroll
;         for (int j = 0; j < 8; ++j) { const LAS float* row = imp + (8 * wid + j) * IMP_LD;
;             { const int kk = lane; const unsigned bits = __float_as_uint(row[kk]);
;               key0[j] = (kk > cur) ? 0u : (kk == 0 || kk == cur || kk == cur - 1) ? (0xFFFFFF80u | (unsigned)(127 - kk)) : ((((bits >> 7) + 1u) << 7) | (unsigned)(127 - kk)); }
;             { const int kk = lane + 64; const unsigned bits = __float_as_uint(row[kk]);
;               key1[j] = (kk > cur) ? 0u : (kk == cur || kk == cur - 1) ? (0xFFFFFF80u | (unsigned)(127 - kk)) : ((((bits >> 7) + 1u) << 7) | (unsigned)(127 - kk)); }
;             w0[j] = 0u; w1[j] = 0u; w2[j] = 0u; w3[j] = 0u; }
.LBB0_632:
	v_writelane_b32 v245, s16, 61
	s_lshl_b64 s[2:3], s[2:3], 11
	v_cmp_eq_u32_e64 s[10:11], 0, v157
	v_writelane_b32 v245, s17, 62
	v_writelane_b32 v245, s2, 63
	v_lshlrev_b32_e32 v9, 2, v157
	v_readlane_b32 s16, v245, 28
	v_writelane_b32 v244, s3, 0
	s_add_i32 s2, s67, -1
	v_cmp_eq_u32_e32 vcc, s2, v157
	s_movk_i32 s2, 0xff80
	v_bitop3_b32 v5, v157, s2, v157 bitop3:0xcf
	s_add_i32 s2, s67, 0xffffffbf
	v_cmp_eq_u32_e64 s[12:13], s2, v157
	s_add_i32 s2, s16, s7
	s_waitcnt lgkmcnt(0)
	v_add_u32_e32 v6, s2, v9
	v_cmp_le_i32_e64 s[14:15], s67, v157
	s_or_b64 s[2:3], s[10:11], vcc
	ds_read2st64_b32 v[6:7], v6 offset1:1
	s_or_b64 vcc, s[2:3], s[14:15]
	v_readlane_b32 s2, v245, 56
	s_or_b32 s7, s2, 1
	s_mul_i32 s2, s7, 0x210
	v_add_u32_e32 v4, 64, v157
	v_cmp_ge_i32_e64 s[14:15], s67, v157
	s_add_i32 s2, s16, s2
	v_add_u32_e32 v20, s2, v9
	v_cndmask_b32_e64 v24, 0, v5, s[14:15]
	v_cmp_le_i32_e64 s[14:15], s67, v4
	s_waitcnt lgkmcnt(0)
	v_and_b32_e32 v5, 0xffffff80, v6
	s_or_b64 s[12:13], s[14:15], s[12:13]
	v_cmp_ge_i32_e64 s[14:15], s67, v4
	v_and_b32_e32 v4, 0xffffff80, v7
	ds_read2st64_b32 v[6:7], v20 offset1:1
	v_add_u32_e32 v9, 32, v20
	ds_read2_b32 v[10:11], v20 offset0:132 offset1:196
	ds_read2st64_b32 v[12:13], v9 offset0:4 offset1:5
	v_sub_u32_e32 v22, 0x7f, v157
	s_waitcnt lgkmcnt(2)
	v_and_b32_e32 v6, 0xffffff80, v6
	v_sub_u32_e32 v23, 63, v157
	v_add_u32_e32 v6, 0x80, v6
	v_or_b32_e32 v8, 0xffffff80, v23
	v_or_b32_e32 v6, v6, v22
	v_cndmask_b32_e64 v25, 0, v8, s[14:15]
	v_cndmask_b32_e32 v8, v6, v24, vcc
	v_and_b32_e32 v6, 0xffffff80, v7
	s_waitcnt lgkmcnt(1)
	v_and_b32_e32 v7, 0xffffff80, v10
	s_waitcnt lgkmcnt(0)
	v_and_b32_e32 v9, 0xffffff80, v12
	v_add_u32_e32 v7, 0x80, v7
	v_add_u32_e32 v9, 0x80, v9
	v_or_b32_e32 v7, v7, v22
	v_or_b32_e32 v9, v9, v22
	v_cndmask_b32_e32 v10, v7, v24, vcc
	v_and_b32_e32 v7, 0xffffff80, v11
	v_cndmask_b32_e32 v12, v9, v24, vcc
	v_and_b32_e32 v9, 0xffffff80, v13
	v_add_u32_e32 v11, 48, v20
	v_add_u32_e32 v13, 64, v20
	ds_read2st64_b32 v[14:15], v11 offset0:6 offset1:7
	ds_read2st64_b32 v[16:17], v13 offset0:8 offset1:9
	v_add_u32_e32 v5, 0x80, v5
	v_add_u32_e32 v4, 0x80, v4
	v_add_u32_e32 v6, 0x80, v6
	s_waitcnt lgkmcnt(1)
	v_and_b32_e32 v11, 0xffffff80, v14
	s_waitcnt lgkmcnt(0)
	v_and_b32_e32 v13, 0xffffff80, v16
	v_add_u32_e32 v11, 0x80, v11
	v_add_u32_e32 v13, 0x80, v13
	v_or_b32_e32 v11, v11, v22
	v_or_b32_e32 v13, v13, v22
	v_cndmask_b32_e32 v14, v11, v24, vcc
	v_and_b32_e32 v11, 0xffffff80, v15
	v_cndmask_b32_e32 v16, v13, v24, vcc
	v_and_b32_e32 v13, 0xffffff80, v17
	v_add_u32_e32 v15, 0x50, v20
	v_add_u32_e32 v17, 0x60, v20
	ds_read2st64_b32 v[18:19], v15 offset0:10 offset1:11
	ds_read2st64_b32 v[20:21], v17 offset0:12 offset1:13
	v_add_u32_e32 v7, 0x80, v7
	v_add_u32_e32 v9, 0x80, v9
	v_add_u32_e32 v11, 0x80, v11
	s_waitcnt lgkmcnt(1)
	v_and_b32_e32 v15, 0xffffff80, v18
	s_waitcnt lgkmcnt(0)
	v_and_b32_e32 v17, 0xffffff80, v20
	v_add_u32_e32 v15, 0x80, v15
	v_add_u32_e32 v17, 0x80, v17
	v_or_b32_e32 v15, v15, v22
	v_or_b32_e32 v17, v17, v22
	v_cndmask_b32_e32 v18, v15, v24, vcc
	v_and_b32_e32 v15, 0xffffff80, v19
	v_cndmask_b32_e32 v19, v17, v24, vcc
	v_and_b32_e32 v17, 0xffffff80, v21
	v_add_u32_e32 v13, 0x80, v13
	v_add_u32_e32 v15, 0x80, v15
	v_add_u32_e32 v17, 0x80, v17
	s_mov_b32 s6, 0
	v_or_b32_e32 v5, v5, v22
	v_or_b32_e32 v4, v4, v23
	v_readlane_b32 s3, v245, 57
	v_or_b32_e32 v6, v6, v23
	v_or_b32_e32 v7, v7, v23
	v_or_b32_e32 v9, v9, v23
	v_or_b32_e32 v11, v11, v23
	v_or_b32_e32 v13, v13, v23
	v_or_b32_e32 v15, v15, v23
	v_or_b32_e32 v17, v17, v23
	v_cndmask_b32_e32 v5, v5, v24, vcc
	v_cndmask_b32_e64 v4, v4, v25, s[12:13]
	v_cndmask_b32_e64 v6, v6, v25, s[12:13]
	v_cndmask_b32_e64 v7, v7, v25, s[12:13]
	v_cndmask_b32_e64 v9, v9, v25, s[12:13]
	v_cndmask_b32_e64 v11, v11, v25, s[12:13]
	v_cndmask_b32_e64 v13, v13, v25, s[12:13]
	v_cndmask_b32_e64 v15, v15, v25, s[12:13]
	v_cndmask_b32_e64 v17, v17, v25, s[12:13]
	s_mov_b32 s36, 0
	s_mov_b32 s37, 0
	s_mov_b32 s38, 0
	s_mov_b32 s39, 0
	s_mov_b32 s40, 0
	s_mov_b32 s41, 0
	s_mov_b32 s42, 0
	s_mov_b32 s43, 0
	s_mov_b32 s44, 0x80000000
	s_mov_b32 s48, 0
	s_mov_b32 s49, 0
	s_mov_b32 s50, 0
	s_mov_b32 s51, 0
; __device__ __forceinline__ void attn_unit(const Frame& F, unsigned char* ws, int g, int qt) {
;     ...
;         for (int it = 0; it < 16; ++it) {
; #pragma unroll
;             for (int j = 0; j < 8; ++j) {
;                 const unsigned M = __reduce_max_sync(~0ull, key0[j] > key1[j] ? key0[j] : key1[j]);
;                 const unsigned kk = 127u - (M & 127u), bit = (M != 0u) ? (1u << (kk & 31u)) : 0u, wq = kk >> 5;
;                 w0[j] |= (wq == 0u) ? bit : 0u; w1[j] |= (wq == 1u) ? bit : 0u; w2[j] |= (wq == 2u) ? bit : 0u; w3[j] |= (wq == 3u) ? bit : 0u;
;                 key0[j] = (key0[j] == M) ? 0u : key0[j]; key1[j] = (key1[j] == M) ? 0u : key1[j];
;             }
;         }
;         if (lane == 0) {
; #pragma unroll
;             for (int j = 0; j < 8; ++j) { const int tj = 8 * wid + j; sel[tj * 4 + 0] = w0[j]; sel[tj * 4 + 1] = w1[j]; sel[tj * 4 + 2] = w2[j]; sel[tj * 4 + 3] = w3[j];
;                 atomicOr((unsigned*)&uni[0], w0[j]); atomicOr((unsigned*)&uni[1], w1[j]); atomicOr((unsigned*)&uni[2], w2[j]); atomicOr((unsigned*)&uni[3], w3[j]); }
;         }
.Ltopk_bit:
	s_or_b32 s45, s36, s44
	s_or_b32 s46, s37, s44
	s_or_b32 s47, s38, s44
	s_or_b32 s52, s39, s44
	v_cmp_le_u32_e64 s[12:13], s45, v5
	v_cmp_le_u32_e64 s[14:15], s45, v4
	v_cmp_le_u32_e64 s[16:17], s46, v8
	v_cmp_le_u32_e64 s[18:19], s46, v6
	v_cmp_le_u32_e64 s[20:21], s47, v10
	v_cmp_le_u32_e64 s[22:23], s47, v7
	v_cmp_le_u32_e64 s[24:25], s52, v12
	v_cmp_le_u32_e64 s[28:29], s52, v9
	s_bcnt1_i32_b64 s12, s[12:13]
	s_bcnt1_i32_b64 s14, s[14:15]
	s_bcnt1_i32_b64 s16, s[16:17]
	s_bcnt1_i32_b64 s18, s[18:19]
	s_add_i32 s12, s12, s14
	s_add_i32 s16, s16, s18
	s_cmp_ge_u32 s12, 16
	s_cselect_b32 s36, s45, s36
	s_cmp_ge_u32 s16, 16
	s_cselect_b32 s37, s46, s37
	s_bcnt1_i32_b64 s20, s[20:21]
	s_bcnt1_i32_b64 s22, s[22:23]
	s_bcnt1_i32_b64 s24, s[24:25]
	s_bcnt1_i32_b64 s28, s[28:29]
	s_add_i32 s20, s20, s22
	s_add_i32 s24, s24, s28
	s_cmp_ge_u32 s20, 16
	s_cselect_b32 s38, s47, s38
	s_cmp_ge_u32 s24, 16
	s_cselect_b32 s39, s52, s39
	s_or_b32 s45, s40, s44
	s_or_b32 s46, s41, s44
	s_or_b32 s47, s42, s44
	s_or_b32 s52, s43, s44
	v_cmp_le_u32_e64 s[12:13], s45, v14
	v_cmp_le_u32_e64 s[14:15], s45, v11
	v_cmp_le_u32_e64 s[16:17], s46, v16
	v_cmp_le_u32_e64 s[18:19], s46, v13
	v_cmp_le_u32_e64 s[20:21], s47, v18
	v_cmp_le_u32_e64 s[22:23], s47, v15
	v_cmp_le_u32_e64 s[24:25], s52, v19
	v_cmp_le_u32_e64 s[28:29], s52, v17
	s_bcnt1_i32_b64 s12, s[12:13]
	s_bcnt1_i32_b64 s14, s[14:15]
	s_bcnt1_i32_b64 s16, s[16:17]
	s_bcnt1_i32_b64 s18, s[18:19]
	s_add_i32 s12, s12, s14
	s_add_i32 s16, s16, s18
	s_cmp_ge_u32 s12, 16
	s_cselect_b32 s40, s45, s40
	s_cmp_ge_u32 s16, 16
	s_cselect_b32 s41, s46, s41
	s_bcnt1_i32_b64 s20, s[20:21]
	s_bcnt1_i32_b64 s22, s[22:23]
	s_bcnt1_i32_b64 s24, s[24:25]
	s_bcnt1_i32_b64 s28, s[28:29]
	s_add_i32 s20, s20, s22
	s_add_i32 s24, s24, s28
	s_cmp_ge_u32 s20, 16
	s_cselect_b32 s42, s47, s42
	s_cmp_ge_u32 s24, 16
	s_cselect_b32 s43, s52, s43
	s_lshr_b32 s44, s44, 1
	s_cmp_lg_u32 s44, 0
	s_cbranch_scc1 .Ltopk_bit
	s_max_u32 s45, s36, 1
	s_max_u32 s46, s37, 1
	s_max_u32 s47, s38, 1
	s_max_u32 s52, s39, 1
	v_cmp_le_u32_e64 s[12:13], s45, v5
	v_cmp_le_u32_e64 s[14:15], s45, v4
	v_cmp_le_u32_e64 s[16:17], s46, v8
	v_cmp_le_u32_e64 s[18:19], s46, v6
	v_cmp_le_u32_e64 s[20:21], s47, v10
	v_cmp_le_u32_e64 s[22:23], s47, v7
	v_cmp_le_u32_e64 s[24:25], s52, v12
	v_cmp_le_u32_e64 s[28:29], s52, v9
	s_nop 1
	v_mov_b32_e32 v20, s12
	v_mov_b32_e32 v21, s13
	v_mov_b32_e32 v22, s14
	v_mov_b32_e32 v23, s15
	s_or_b32 s48, s48, s12
	s_or_b32 s49, s49, s13
	s_or_b32 s50, s50, s14
	s_or_b32 s51, s51, s15
	v_mov_b32_e32 v24, s16
	v_mov_b32_e32 v25, s17
	v_mov_b32_e32 v26, s18
	v_mov_b32_e32 v27, s19
	s_or_b32 s48, s48, s16
	s_or_b32 s49, s49, s17
	s_or_b32 s50, s50, s18
	s_or_b32 s51, s51, s19
	v_mov_b32_e32 v28, s20
	v_mov_b32_e32 v29, s21
	v_mov_b32_e32 v30, s22
	v_mov_b32_e32 v31, s23
	s_or_b32 s48, s48, s20
	s_or_b32 s49, s49, s21
	s_or_b32 s50, s50, s22
	s_or_b32 s51, s51, s23
	v_mov_b32_e32 v32, s24
	v_mov_b32_e32 v33, s25
	v_mov_b32_e32 v34, s28
	v_mov_b32_e32 v35, s29
	s_or_b32 s48, s48, s24
	s_or_b32 s49, s49, s25
	s_or_b32 s50, s50, s28
	s_or_b32 s51, s51, s29
	s_max_u32 s45, s40, 1
	s_max_u32 s46, s41, 1
	s_max_u32 s47, s42, 1
	s_max_u32 s52, s43, 1
	v_cmp_le_u32_e64 s[12:13], s45, v14
	v_cmp_le_u32_e64 s[14:15], s45, v11
	v_cmp_le_u32_e64 s[16:17], s46, v16
	v_cmp_le_u32_e64 s[18:19], s46, v13
	v_cmp_le_u32_e64 s[20:21], s47, v18
	v_cmp_le_u32_e64 s[22:23], s47, v15
	v_cmp_le_u32_e64 s[24:25], s52, v19
	v_cmp_le_u32_e64 s[28:29], s52, v17
	s_nop 1
	v_mov_b32_e32 v44, s12
	v_mov_b32_e32 v45, s13
	v_mov_b32_e32 v46, s14
	v_mov_b32_e32 v47, s15
	s_or_b32 s48, s48, s12
	s_or_b32 s49, s49, s13
	s_or_b32 s50, s50, s14
	s_or_b32 s51, s51, s15
	v_mov_b32_e32 v48, s16
	v_mov_b32_e32 v49, s17
	v_mov_b32_e32 v50, s18
	v_mov_b32_e32 v51, s19
	s_or_b32 s48, s48, s16
	s_or_b32 s49, s49, s17
	s_or_b32 s50, s50, s18
	s_or_b32 s51, s51, s19
	v_mov_b32_e32 v52, s20
	v_mov_b32_e32 v53, s21
	v_mov_b32_e32 v54, s22
	v_mov_b32_e32 v55, s23
	s_or_b32 s48, s48, s20
	s_or_b32 s49, s49, s21
	s_or_b32 s50, s50, s22
	s_or_b32 s51, s51, s23
	v_mov_b32_e32 v56, s24
	v_mov_b32_e32 v57, s25
	v_mov_b32_e32 v58, s28
	v_mov_b32_e32 v59, s29
	s_or_b32 s48, s48, s24
	s_or_b32 s49, s49, s25
	s_or_b32 s50, s50, s28
	s_or_b32 s51, s51, s29
	s_lshl_b32 s12, s30, 7
	s_add_i32 s12, s12, 0x20c00
	s_and_saveexec_b64 s[26:27], s[10:11]
	v_mov_b32_e32 v36, s12
	ds_write_b128 v36, v[20:23]
	ds_write_b128 v36, v[24:27] offset:16
	ds_write_b128 v36, v[28:31] offset:32
	ds_write_b128 v36, v[32:35] offset:48
	ds_write_b128 v36, v[44:47] offset:64
	ds_write_b128 v36, v[48:51] offset:80
	ds_write_b128 v36, v[52:55] offset:96
	ds_write_b128 v36, v[56:59] offset:112
	v_mov_b32_e32 v37, 0x21000
	v_mov_b32_e32 v38, s48
	v_mov_b32_e32 v39, s49
	v_mov_b32_e32 v60, s50
	v_mov_b32_e32 v61, s51
	ds_or_b32 v37, v38
	ds_or_b32 v37, v39 offset:4
	ds_or_b32 v37, v60 offset:8
	ds_or_b32 v37, v61 offset:12
